# in-projection GEMM epilogue stores marked nt (streaming) on top of prep-loop rewrite and new conversion queue
# baseline (speedup 1.0000x reference)
.LBB0_85:
	ds_read_b128 v[154:157], v150
	ds_read_b128 v[158:161], v150 offset:1024
	ds_read_b128 v[162:165], v150 offset:2048
	ds_read_b128 v[166:169], v150 offset:3072
	s_add_u32 s60, s24, 0xfff80080
	s_addc_u32 s61, s25, -1
	s_cmp_eq_u32 s59, 28
	s_cselect_b32 s87, s15, s61
	s_cselect_b32 s86, s55, s60
	s_cselect_b32 s85, s13, s58
	s_cselect_b32 s84, s56, s57
	v_lshl_add_u64 v[202:203], s[24:25], 0, v[138:139]
	s_add_i32 m0, s11, 0xc000
	ds_read_b128 v[170:173], v151
	ds_read_b128 v[174:177], v151 offset:1024
	ds_read_b128 v[178:181], v151 offset:2048
	ds_read_b128 v[182:185], v151 offset:3072
	ds_read_b128 v[186:189], v151 offset:4096
	ds_read_b128 v[190:193], v151 offset:5120
	ds_read_b128 v[194:197], v151 offset:6144
	ds_read_b128 v[198:201], v151 offset:7168
	global_load_lds_dwordx4 v[202:203], off
	v_lshl_add_u64 v[202:203], s[24:25], 0, v[140:141]
	s_add_i32 m0, s11, 0xe000
	s_nop 0
	global_load_lds_dwordx4 v[202:203], off
	s_waitcnt lgkmcnt(8)
	s_barrier
	s_waitcnt lgkmcnt(0)
	s_setprio 1
	s_waitcnt lgkmcnt(0)
	v_mfma_f32_16x16x32_bf16 v[126:129], v[154:157], v[170:173], v[126:129]
	v_mfma_f32_16x16x32_bf16 v[122:125], v[162:165], v[170:173], v[122:125]
	v_mfma_f32_16x16x32_bf16 v[118:121], v[154:157], v[178:181], v[118:121]
	v_mfma_f32_16x16x32_bf16 v[114:117], v[162:165], v[178:181], v[114:117]
	v_mfma_f32_16x16x32_bf16 v[102:105], v[154:157], v[186:189], v[102:105]
	v_mfma_f32_16x16x32_bf16 v[98:101], v[162:165], v[186:189], v[98:101]
	v_mfma_f32_16x16x32_bf16 v[86:89], v[154:157], v[194:197], v[86:89]
	v_mfma_f32_16x16x32_bf16 v[82:85], v[162:165], v[194:197], v[82:85]
	v_mfma_f32_16x16x32_bf16 v[126:129], v[158:161], v[174:177], v[126:129]
	v_mfma_f32_16x16x32_bf16 v[122:125], v[166:169], v[174:177], v[122:125]
	v_mfma_f32_16x16x32_bf16 v[118:121], v[158:161], v[182:185], v[118:121]
	v_mfma_f32_16x16x32_bf16 v[114:117], v[166:169], v[182:185], v[114:117]
	v_mfma_f32_16x16x32_bf16 v[102:105], v[158:161], v[190:193], v[102:105]
	v_mfma_f32_16x16x32_bf16 v[98:101], v[166:169], v[190:193], v[98:101]
	v_mfma_f32_16x16x32_bf16 v[86:89], v[158:161], v[198:201], v[86:89]
	v_mfma_f32_16x16x32_bf16 v[82:85], v[166:169], v[198:201], v[82:85]
	s_setprio 0
	s_barrier
	s_add_i32 s60, s41, s18
	v_lshl_add_u64 v[218:219], s[84:85], 0, v[134:135]
	s_mov_b32 m0, s60
	ds_read_b128 v[202:205], v152
	ds_read_b128 v[206:209], v152 offset:1024
	ds_read_b128 v[210:213], v152 offset:2048
	ds_read_b128 v[214:217], v152 offset:3072
	global_load_lds_dwordx4 v[218:219], off
	v_lshl_add_u64 v[220:221], s[84:85], 0, v[130:131]
	s_add_i32 m0, s60, 0x2000
	s_nop 0
	global_load_lds_dwordx4 v[220:221], off
	s_barrier
	s_waitcnt lgkmcnt(0)
	s_setprio 1
	s_waitcnt lgkmcnt(0)
	v_mfma_f32_16x16x32_bf16 v[110:113], v[202:205], v[170:173], v[110:113]
	v_mfma_f32_16x16x32_bf16 v[106:109], v[210:213], v[170:173], v[106:109]
	v_mfma_f32_16x16x32_bf16 v[94:97], v[202:205], v[178:181], v[94:97]
	v_mfma_f32_16x16x32_bf16 v[90:93], v[210:213], v[178:181], v[90:93]
	v_mfma_f32_16x16x32_bf16 v[78:81], v[202:205], v[186:189], v[78:81]
	v_mfma_f32_16x16x32_bf16 v[74:77], v[210:213], v[186:189], v[74:77]
	v_mfma_f32_16x16x32_bf16 v[70:73], v[202:205], v[194:197], v[70:73]
	v_mfma_f32_16x16x32_bf16 v[66:69], v[210:213], v[194:197], v[66:69]
	v_mfma_f32_16x16x32_bf16 v[110:113], v[206:209], v[174:177], v[110:113]
	v_mfma_f32_16x16x32_bf16 v[106:109], v[214:217], v[174:177], v[106:109]
	v_mfma_f32_16x16x32_bf16 v[94:97], v[206:209], v[182:185], v[94:97]
	v_mfma_f32_16x16x32_bf16 v[90:93], v[214:217], v[182:185], v[90:93]
	v_mfma_f32_16x16x32_bf16 v[78:81], v[206:209], v[190:193], v[78:81]
	v_mfma_f32_16x16x32_bf16 v[74:77], v[214:217], v[190:193], v[74:77]
	v_mfma_f32_16x16x32_bf16 v[70:73], v[206:209], v[198:201], v[70:73]
	v_mfma_f32_16x16x32_bf16 v[66:69], v[214:217], v[198:201], v[66:69]
	s_setprio 0
	s_mov_b32 m0, s11
	v_lshl_add_u64 v[222:223], s[86:87], 0, v[136:137]
	s_barrier
	ds_read_b128 v[170:173], v151 offset:16384
	ds_read_b128 v[174:177], v151 offset:17408
	ds_read_b128 v[178:181], v151 offset:18432
	ds_read_b128 v[182:185], v151 offset:19456
	ds_read_b128 v[186:189], v151 offset:20480
	ds_read_b128 v[190:193], v151 offset:21504
	ds_read_b128 v[194:197], v151 offset:22528
	ds_read_b128 v[198:201], v151 offset:23552
	global_load_lds_dwordx4 v[222:223], off
	v_lshl_add_u64 v[224:225], s[86:87], 0, v[132:133]
	s_mov_b32 m0, s21
	s_nop 0
	global_load_lds_dwordx4 v[224:225], off
	s_barrier
	s_waitcnt lgkmcnt(0)
	s_setprio 1
	s_waitcnt lgkmcnt(0)
	v_mfma_f32_16x16x32_bf16 v[62:65], v[154:157], v[170:173], v[62:65]
	v_mfma_f32_16x16x32_bf16 v[58:61], v[162:165], v[170:173], v[58:61]
	v_mfma_f32_16x16x32_bf16 v[54:57], v[154:157], v[178:181], v[54:57]
	v_mfma_f32_16x16x32_bf16 v[50:53], v[162:165], v[178:181], v[50:53]
	v_mfma_f32_16x16x32_bf16 v[38:41], v[154:157], v[186:189], v[38:41]
	v_mfma_f32_16x16x32_bf16 v[34:37], v[162:165], v[186:189], v[34:37]
	v_mfma_f32_16x16x32_bf16 v[22:25], v[154:157], v[194:197], v[22:25]
	v_mfma_f32_16x16x32_bf16 v[18:21], v[162:165], v[194:197], v[18:21]
	v_mfma_f32_16x16x32_bf16 v[62:65], v[158:161], v[174:177], v[62:65]
	v_mfma_f32_16x16x32_bf16 v[58:61], v[166:169], v[174:177], v[58:61]
	v_mfma_f32_16x16x32_bf16 v[54:57], v[158:161], v[182:185], v[54:57]
	v_mfma_f32_16x16x32_bf16 v[50:53], v[166:169], v[182:185], v[50:53]
	v_mfma_f32_16x16x32_bf16 v[38:41], v[158:161], v[190:193], v[38:41]
	v_mfma_f32_16x16x32_bf16 v[34:37], v[166:169], v[190:193], v[34:37]
	v_mfma_f32_16x16x32_bf16 v[22:25], v[158:161], v[198:201], v[22:25]
	v_mfma_f32_16x16x32_bf16 v[18:21], v[166:169], v[198:201], v[18:21]
	s_setprio 0
	s_barrier
	s_add_u32 s60, s84, 0x80000
	s_addc_u32 s61, s85, 0
	s_add_i32 s62, s52, s18
	v_lshl_add_u64 v[154:155], s[60:61], 0, v[134:135]
	s_mov_b32 m0, s62
	s_nop 0
	global_load_lds_dwordx4 v[154:155], off
	v_lshl_add_u64 v[154:155], s[60:61], 0, v[130:131]
	s_add_i32 m0, s62, 0x2000
	s_nop 0
	global_load_lds_dwordx4 v[154:155], off
	s_waitcnt vmcnt(6)
	s_barrier
	s_setprio 1
	v_mfma_f32_16x16x32_bf16 v[46:49], v[202:205], v[170:173], v[46:49]
	v_mfma_f32_16x16x32_bf16 v[42:45], v[210:213], v[170:173], v[42:45]
	v_mfma_f32_16x16x32_bf16 v[30:33], v[202:205], v[178:181], v[30:33]
	v_mfma_f32_16x16x32_bf16 v[26:29], v[210:213], v[178:181], v[26:29]
	v_mfma_f32_16x16x32_bf16 v[14:17], v[202:205], v[186:189], v[14:17]
	v_mfma_f32_16x16x32_bf16 v[10:13], v[210:213], v[186:189], v[10:13]
	v_mfma_f32_16x16x32_bf16 v[6:9], v[202:205], v[194:197], v[6:9]
	v_mfma_f32_16x16x32_bf16 v[2:5], v[210:213], v[194:197], v[2:5]
	v_mfma_f32_16x16x32_bf16 v[46:49], v[206:209], v[174:177], v[46:49]
	v_mfma_f32_16x16x32_bf16 v[42:45], v[214:217], v[174:177], v[42:45]
	v_mfma_f32_16x16x32_bf16 v[30:33], v[206:209], v[182:185], v[30:33]
	v_mfma_f32_16x16x32_bf16 v[26:29], v[214:217], v[182:185], v[26:29]
	v_mfma_f32_16x16x32_bf16 v[14:17], v[206:209], v[190:193], v[14:17]
	v_mfma_f32_16x16x32_bf16 v[10:13], v[214:217], v[190:193], v[10:13]
	v_mfma_f32_16x16x32_bf16 v[6:9], v[206:209], v[198:201], v[6:9]
	v_mfma_f32_16x16x32_bf16 v[2:5], v[214:217], v[198:201], v[2:5]
	s_setprio 0
	s_add_i32 s62, 0, 0x18000
	v_add_u32_e32 v1, s62, v148
	s_barrier
	ds_read_b128 v[154:157], v1
	ds_read_b128 v[158:161], v1 offset:1024
	ds_read_b128 v[162:165], v1 offset:2048
	ds_read_b128 v[166:169], v1 offset:3072
	s_add_u32 s60, s86, 0x80000
	s_addc_u32 s61, s87, 0
	s_mov_b32 m0, s26
	v_lshl_add_u64 v[202:203], s[60:61], 0, v[136:137]
	ds_read_b128 v[170:173], v151 offset:32768
	ds_read_b128 v[174:177], v151 offset:33792
	ds_read_b128 v[178:181], v151 offset:34816
	ds_read_b128 v[182:185], v151 offset:35840
	ds_read_b128 v[186:189], v151 offset:36864
	ds_read_b128 v[190:193], v151 offset:37888
	ds_read_b128 v[194:197], v151 offset:38912
	ds_read_b128 v[198:201], v151 offset:39936
	global_load_lds_dwordx4 v[202:203], off
	v_lshl_add_u64 v[202:203], s[60:61], 0, v[132:133]
	s_mov_b32 m0, s27
	s_nop 0
	global_load_lds_dwordx4 v[202:203], off
	s_waitcnt lgkmcnt(8)
	s_barrier
	s_waitcnt lgkmcnt(0)
	s_setprio 1
	s_waitcnt lgkmcnt(0)
	v_mfma_f32_16x16x32_bf16 v[126:129], v[154:157], v[170:173], v[126:129]
	v_mfma_f32_16x16x32_bf16 v[122:125], v[162:165], v[170:173], v[122:125]
	v_mfma_f32_16x16x32_bf16 v[118:121], v[154:157], v[178:181], v[118:121]
	v_mfma_f32_16x16x32_bf16 v[114:117], v[162:165], v[178:181], v[114:117]
	v_mfma_f32_16x16x32_bf16 v[102:105], v[154:157], v[186:189], v[102:105]
	v_mfma_f32_16x16x32_bf16 v[98:101], v[162:165], v[186:189], v[98:101]
	v_mfma_f32_16x16x32_bf16 v[86:89], v[154:157], v[194:197], v[86:89]
	v_mfma_f32_16x16x32_bf16 v[82:85], v[162:165], v[194:197], v[82:85]
	v_mfma_f32_16x16x32_bf16 v[126:129], v[158:161], v[174:177], v[126:129]
	v_mfma_f32_16x16x32_bf16 v[122:125], v[166:169], v[174:177], v[122:125]
	v_mfma_f32_16x16x32_bf16 v[118:121], v[158:161], v[182:185], v[118:121]
	v_mfma_f32_16x16x32_bf16 v[114:117], v[166:169], v[182:185], v[114:117]
	v_mfma_f32_16x16x32_bf16 v[102:105], v[158:161], v[190:193], v[102:105]
	v_mfma_f32_16x16x32_bf16 v[98:101], v[166:169], v[190:193], v[98:101]
	v_mfma_f32_16x16x32_bf16 v[86:89], v[158:161], v[198:201], v[86:89]
	v_mfma_f32_16x16x32_bf16 v[82:85], v[166:169], v[198:201], v[82:85]
	s_setprio 0
	s_barrier
	s_add_i32 s63, 0, 0x1c000
	s_add_i32 s60, s62, s18
	v_add_u32_e32 v1, s63, v148
	v_lshl_add_u64 v[218:219], v[218:219], 0, s[8:9]
	s_mov_b32 m0, s60
	ds_read_b128 v[202:205], v1
	ds_read_b128 v[206:209], v1 offset:1024
	ds_read_b128 v[210:213], v1 offset:2048
	ds_read_b128 v[214:217], v1 offset:3072
	global_load_lds_dwordx4 v[218:219], off
	v_lshl_add_u64 v[218:219], v[220:221], 0, s[8:9]
	s_add_i32 m0, s60, 0x2000
	s_nop 0
	global_load_lds_dwordx4 v[218:219], off
	s_barrier
	s_waitcnt lgkmcnt(0)
	s_setprio 1
	s_waitcnt lgkmcnt(0)
	v_mfma_f32_16x16x32_bf16 v[110:113], v[202:205], v[170:173], v[110:113]
	v_mfma_f32_16x16x32_bf16 v[106:109], v[210:213], v[170:173], v[106:109]
	v_mfma_f32_16x16x32_bf16 v[94:97], v[202:205], v[178:181], v[94:97]
	v_mfma_f32_16x16x32_bf16 v[90:93], v[210:213], v[178:181], v[90:93]
	v_mfma_f32_16x16x32_bf16 v[78:81], v[202:205], v[186:189], v[78:81]
	v_mfma_f32_16x16x32_bf16 v[74:77], v[210:213], v[186:189], v[74:77]
	v_mfma_f32_16x16x32_bf16 v[70:73], v[202:205], v[194:197], v[70:73]
	v_mfma_f32_16x16x32_bf16 v[66:69], v[210:213], v[194:197], v[66:69]
	v_mfma_f32_16x16x32_bf16 v[110:113], v[206:209], v[174:177], v[110:113]
	v_mfma_f32_16x16x32_bf16 v[106:109], v[214:217], v[174:177], v[106:109]
	v_mfma_f32_16x16x32_bf16 v[94:97], v[206:209], v[182:185], v[94:97]
	v_mfma_f32_16x16x32_bf16 v[90:93], v[214:217], v[182:185], v[90:93]
	v_mfma_f32_16x16x32_bf16 v[78:81], v[206:209], v[190:193], v[78:81]
	v_mfma_f32_16x16x32_bf16 v[74:77], v[214:217], v[190:193], v[74:77]
	v_mfma_f32_16x16x32_bf16 v[70:73], v[206:209], v[198:201], v[70:73]
	v_mfma_f32_16x16x32_bf16 v[66:69], v[214:217], v[198:201], v[66:69]
	s_setprio 0
	s_mov_b32 m0, s34
	v_lshl_add_u64 v[218:219], v[222:223], 0, s[8:9]
	s_barrier
	ds_read_b128 v[170:173], v151 offset:49152
	ds_read_b128 v[174:177], v151 offset:50176
	ds_read_b128 v[178:181], v151 offset:51200
	ds_read_b128 v[182:185], v151 offset:52224
	ds_read_b128 v[186:189], v151 offset:53248
	ds_read_b128 v[190:193], v151 offset:54272
	ds_read_b128 v[194:197], v151 offset:55296
	ds_read_b128 v[198:201], v151 offset:56320
	global_load_lds_dwordx4 v[218:219], off
	v_lshl_add_u64 v[218:219], v[224:225], 0, s[8:9]
	s_mov_b32 m0, s35
	s_nop 0
	global_load_lds_dwordx4 v[218:219], off
	s_barrier
	s_waitcnt lgkmcnt(0)
	s_setprio 1
	s_waitcnt lgkmcnt(0)
	v_mfma_f32_16x16x32_bf16 v[62:65], v[154:157], v[170:173], v[62:65]
	v_mfma_f32_16x16x32_bf16 v[58:61], v[162:165], v[170:173], v[58:61]
	v_mfma_f32_16x16x32_bf16 v[54:57], v[154:157], v[178:181], v[54:57]
	v_mfma_f32_16x16x32_bf16 v[50:53], v[162:165], v[178:181], v[50:53]
	v_mfma_f32_16x16x32_bf16 v[38:41], v[154:157], v[186:189], v[38:41]
	v_mfma_f32_16x16x32_bf16 v[34:37], v[162:165], v[186:189], v[34:37]
	v_mfma_f32_16x16x32_bf16 v[22:25], v[154:157], v[194:197], v[22:25]
	v_mfma_f32_16x16x32_bf16 v[18:21], v[162:165], v[194:197], v[18:21]
	v_mfma_f32_16x16x32_bf16 v[62:65], v[158:161], v[174:177], v[62:65]
	v_mfma_f32_16x16x32_bf16 v[58:61], v[166:169], v[174:177], v[58:61]
	v_mfma_f32_16x16x32_bf16 v[54:57], v[158:161], v[182:185], v[54:57]
	v_mfma_f32_16x16x32_bf16 v[50:53], v[166:169], v[182:185], v[50:53]
	v_mfma_f32_16x16x32_bf16 v[38:41], v[158:161], v[190:193], v[38:41]
	v_mfma_f32_16x16x32_bf16 v[34:37], v[166:169], v[190:193], v[34:37]
	v_mfma_f32_16x16x32_bf16 v[22:25], v[158:161], v[198:201], v[22:25]
	v_mfma_f32_16x16x32_bf16 v[18:21], v[166:169], v[198:201], v[18:21]
	s_setprio 0
	s_barrier
	s_add_u32 s60, s84, 0x80080
	s_addc_u32 s61, s85, 0
	s_add_i32 s62, s63, s18
	v_lshl_add_u64 v[154:155], s[60:61], 0, v[134:135]
	s_mov_b32 m0, s62
	s_nop 0
	global_load_lds_dwordx4 v[154:155], off
	v_lshl_add_u64 v[154:155], s[60:61], 0, v[130:131]
	s_add_i32 m0, s62, 0x2000
	s_nop 0
	global_load_lds_dwordx4 v[154:155], off
	s_waitcnt vmcnt(6)
	s_barrier
	s_setprio 1
	v_mfma_f32_16x16x32_bf16 v[46:49], v[202:205], v[170:173], v[46:49]
	v_mfma_f32_16x16x32_bf16 v[42:45], v[210:213], v[170:173], v[42:45]
	v_mfma_f32_16x16x32_bf16 v[30:33], v[202:205], v[178:181], v[30:33]
	v_mfma_f32_16x16x32_bf16 v[26:29], v[210:213], v[178:181], v[26:29]
	v_mfma_f32_16x16x32_bf16 v[14:17], v[202:205], v[186:189], v[14:17]
	v_mfma_f32_16x16x32_bf16 v[10:13], v[210:213], v[186:189], v[10:13]
	v_mfma_f32_16x16x32_bf16 v[6:9], v[202:205], v[194:197], v[6:9]
	v_mfma_f32_16x16x32_bf16 v[2:5], v[210:213], v[194:197], v[2:5]
	v_mfma_f32_16x16x32_bf16 v[46:49], v[206:209], v[174:177], v[46:49]
	v_mfma_f32_16x16x32_bf16 v[42:45], v[214:217], v[174:177], v[42:45]
	v_mfma_f32_16x16x32_bf16 v[30:33], v[206:209], v[182:185], v[30:33]
	v_mfma_f32_16x16x32_bf16 v[26:29], v[214:217], v[182:185], v[26:29]
	v_mfma_f32_16x16x32_bf16 v[14:17], v[206:209], v[190:193], v[14:17]
	v_mfma_f32_16x16x32_bf16 v[10:13], v[214:217], v[190:193], v[10:13]
	v_mfma_f32_16x16x32_bf16 v[6:9], v[206:209], v[198:201], v[6:9]
	v_mfma_f32_16x16x32_bf16 v[2:5], v[214:217], v[198:201], v[2:5]
	s_setprio 0
	s_add_i32 s59, s59, 2
	s_add_u32 s24, s24, 0x100
	s_addc_u32 s25, s25, 0
	s_add_u32 s57, s57, 0x100
	s_addc_u32 s58, s58, 0
	s_cmp_gt_u32 s59, 29
	s_barrier
	s_cbranch_scc0 .LBB0_85
	v_lshl_add_u32 v1, s10, 8, v147
	v_lshl_or_b32 v154, s54, 8, v149
	v_ashrrev_i32_e32 v155, 31, v154
	v_mov_b64_e32 v[156:157], s[96:97]
	v_cvt_pk_bf16_f32 v70, v70, v71
	v_cvt_pk_bf16_f32 v71, v72, v73
	v_cvt_pk_bf16_f32 v72, v66, v67
	v_add_u32_e32 v66, 0x80, v1
	v_mad_i64_i32 v[158:159], s[24:25], v1, s53, v[156:157]
	v_lshlrev_b64 v[154:155], 1, v[154:155]
	v_cvt_pk_bf16_f32 v110, v110, v111
	v_cvt_pk_bf16_f32 v111, v112, v113
	v_cvt_pk_bf16_f32 v112, v106, v107
	v_or_b32_e32 v106, 16, v1
	v_mad_i64_i32 v[66:67], s[24:25], v66, s53, v[156:157]
	v_cvt_pk_bf16_f32 v46, v46, v47
	v_cvt_pk_bf16_f32 v47, v48, v49
	v_cvt_pk_bf16_f32 v48, v42, v43
	v_add_u32_e32 v42, 0x90, v1
	v_lshl_add_u64 v[158:159], v[158:159], 0, v[154:155]
	v_cvt_pk_bf16_f32 v113, v108, v109
	v_mad_i64_i32 v[106:107], s[24:25], v106, s53, v[156:157]
	v_cvt_pk_bf16_f32 v94, v94, v95
	v_cvt_pk_bf16_f32 v95, v96, v97
	v_cvt_pk_bf16_f32 v96, v90, v91
	v_or_b32_e32 v90, 32, v1
	v_lshl_add_u64 v[66:67], v[66:67], 0, v[154:155]
	v_cvt_pk_bf16_f32 v49, v44, v45
	v_mad_i64_i32 v[42:43], s[24:25], v42, s53, v[156:157]
	v_cvt_pk_bf16_f32 v30, v30, v31
	v_cvt_pk_bf16_f32 v31, v32, v33
	v_cvt_pk_bf16_f32 v32, v26, v27
	v_add_u32_e32 v26, 0xa0, v1
	global_store_dwordx4 v[158:159], v[110:113], off offset:256 nt
	v_cvt_pk_bf16_f32 v97, v92, v93
	v_mad_i64_i32 v[90:91], s[24:25], v90, s53, v[156:157]
	v_lshl_add_u64 v[110:111], v[106:107], 0, v[154:155]
	v_cvt_pk_bf16_f32 v78, v78, v79
	v_cvt_pk_bf16_f32 v79, v80, v81
	v_cvt_pk_bf16_f32 v80, v74, v75
	v_or_b32_e32 v74, 48, v1
	global_store_dwordx4 v[66:67], v[46:49], off offset:256 nt
	v_cvt_pk_bf16_f32 v33, v28, v29
	v_mad_i64_i32 v[26:27], s[24:25], v26, s53, v[156:157]
	v_lshl_add_u64 v[46:47], v[42:43], 0, v[154:155]
	v_add_u32_e32 v1, 0xb0, v1
	global_store_dwordx4 v[110:111], v[94:97], off offset:256 nt
	v_cvt_pk_bf16_f32 v81, v76, v77
	v_mad_i64_i32 v[74:75], s[24:25], v74, s53, v[156:157]
	v_lshl_add_u64 v[94:95], v[90:91], 0, v[154:155]
	global_store_dwordx4 v[46:47], v[30:33], off offset:256 nt
	v_cvt_pk_bf16_f32 v14, v14, v15
	v_cvt_pk_bf16_f32 v15, v16, v17
	v_lshl_add_u64 v[30:31], v[26:27], 0, v[154:155]
	v_cvt_pk_bf16_f32 v16, v10, v11
	v_cvt_pk_bf16_f32 v17, v12, v13
	v_mad_i64_i32 v[10:11], s[24:25], v1, s53, v[156:157]
	v_cvt_pk_bf16_f32 v126, v126, v127
	v_cvt_pk_bf16_f32 v127, v128, v129
	v_cvt_pk_bf16_f32 v128, v122, v123
	v_cvt_pk_bf16_f32 v129, v124, v125
	v_cvt_pk_bf16_f32 v106, v118, v119
	v_cvt_pk_bf16_f32 v107, v120, v121
	v_cvt_pk_bf16_f32 v108, v114, v115
	v_cvt_pk_bf16_f32 v109, v116, v117
	v_cvt_pk_bf16_f32 v90, v102, v103
	v_cvt_pk_bf16_f32 v91, v104, v105
	v_cvt_pk_bf16_f32 v92, v98, v99
	v_cvt_pk_bf16_f32 v93, v100, v101
	global_store_dwordx4 v[94:95], v[78:81], off offset:256 nt
	v_cvt_pk_bf16_f32 v76, v82, v83
	v_cvt_pk_bf16_f32 v77, v84, v85
	v_lshl_add_u64 v[78:79], v[74:75], 0, v[154:155]
	v_cvt_pk_bf16_f32 v74, v86, v87
	v_cvt_pk_bf16_f32 v75, v88, v89
	v_cvt_pk_bf16_f32 v73, v68, v69
	v_cvt_pk_bf16_f32 v62, v62, v63
	v_cvt_pk_bf16_f32 v63, v64, v65
	v_cvt_pk_bf16_f32 v64, v58, v59
	v_cvt_pk_bf16_f32 v65, v60, v61
	v_cvt_pk_bf16_f32 v42, v54, v55
	v_cvt_pk_bf16_f32 v43, v56, v57
	v_cvt_pk_bf16_f32 v44, v50, v51
	v_cvt_pk_bf16_f32 v45, v52, v53
	v_cvt_pk_bf16_f32 v26, v38, v39
	v_cvt_pk_bf16_f32 v27, v40, v41
	v_cvt_pk_bf16_f32 v28, v34, v35
	v_cvt_pk_bf16_f32 v29, v36, v37
	global_store_dwordx4 v[30:31], v[14:17], off offset:256 nt
	v_cvt_pk_bf16_f32 v12, v18, v19
	v_cvt_pk_bf16_f32 v13, v20, v21
	v_lshl_add_u64 v[14:15], v[10:11], 0, v[154:155]
	v_cvt_pk_bf16_f32 v10, v22, v23
	v_cvt_pk_bf16_f32 v11, v24, v25
	v_cvt_pk_bf16_f32 v6, v6, v7
	v_cvt_pk_bf16_f32 v7, v8, v9
	v_cvt_pk_bf16_f32 v8, v2, v3
	v_cvt_pk_bf16_f32 v9, v4, v5
	s_and_b64 vcc, exec, s[0:1]
	s_mov_b32 s54, s12
	s_mov_b32 s10, s14
	s_mov_b64 s[84:85], s[22:23]
	s_mov_b64 s[24:25], s[16:17]
	v_readlane_b32 s93, v254, 9
	global_store_dwordx4 v[158:159], v[126:129], off nt
	global_store_dwordx4 v[110:111], v[106:109], off nt
	global_store_dwordx4 v[94:95], v[90:93], off nt
	global_store_dwordx4 v[78:79], v[74:77], off nt
	global_store_dwordx4 v[78:79], v[70:73], off offset:256 nt
	global_store_dwordx4 v[66:67], v[62:65], off nt
	global_store_dwordx4 v[46:47], v[42:45], off nt
	global_store_dwordx4 v[30:31], v[26:29], off nt
	global_store_dwordx4 v[14:15], v[10:13], off nt
	global_store_dwordx4 v[14:15], v[6:9], off offset:256 nt
	s_cbranch_vccz .LBB0_82
	s_waitcnt vmcnt(0)
	s_cmpk_gt_u32 s3, 0xff
	s_cbranch_scc1 .LBB0_89
	s_barrier
